# attention unit prologue: dropped the dead default K-piece copy and the two memory waits it and the loop-exit state forced at unit start; next-unit ticket prefetch
# baseline (speedup 1.0000x reference)
.LBB0_956:
	s_or_b64 exec, exec, s[14:15]
	v_mov_b32_e32 v16, s48
	s_waitcnt lgkmcnt(0)
	s_barrier
	ds_read_b32 v16, v16
	s_mov_b64 s[14:15], -1
	s_waitcnt lgkmcnt(0)
	v_readfirstlane_b32 s24, v16
	s_cmpk_gt_i32 s24, 0x1ff
	s_cbranch_scc1 .LBB0_951
	s_mov_b32 s39, 1
	s_and_b32 s26, s24, 31
	s_mul_i32 s14, s26, 0xc0000
	s_add_u32 s16, s20, s14
	s_addc_u32 s17, s21, 0
	v_lshl_add_u64 v[16:17], s[16:17], 0, v[174:175]
	v_lshl_add_u64 v[104:105], v[166:167], 1, v[16:17]
	global_load_dwordx4 v[92:95], v[104:105], off
	s_mov_b32 s15, s65
	s_and_saveexec_b64 s[18:19], s[2:3]
	s_cbranch_execz .LBB0_959
	v_lshl_add_u64 v[16:17], s[16:17], 0, v[176:177]
	v_lshl_add_u64 v[16:17], v[170:171], 1, v[16:17]
	global_load_dwordx4 v[80:83], v[16:17], off
.LBB0_959:
	s_or_b64 exec, exec, s[18:19]
	s_lshl_b32 s64, s26, 19
	v_lshl_add_u64 v[198:199], v[190:191], 0, s[64:65]
	v_add_co_u32_e32 v16, vcc, 0x3000, v104
	v_addc_co_u32_e32 v17, vcc, 0, v105, vcc
	global_load_dwordx4 v[84:87], v[198:199], off
	global_load_dwordx4 v[96:99], v[16:17], off
	s_and_saveexec_b64 s[18:19], s[2:3]
	s_cbranch_execz .LBB0_961
	v_lshl_add_u64 v[16:17], s[16:17], 0, v[178:179]
	v_lshl_add_u64 v[16:17], v[170:171], 1, v[16:17]
	global_load_dwordx4 v[48:51], v[16:17], off
